# baseline (speedup 1.0000x reference)
_Z11prep_kernelPKfS0_S0_S0_S0_S0_S0_S0_S0_PKiPDv8_DF16bS4_PfS5_S5_PiPt:
	s_load_dwordx4 s[16:19], s[0:1], 0x0
	s_load_dwordx4 s[20:23], s[0:1], 0x10
	s_load_dwordx4 s[24:27], s[0:1], 0x20
	s_load_dwordx4 s[28:31], s[0:1], 0x30
	s_load_dwordx4 s[32:35], s[0:1], 0x40
	s_load_dwordx2 s[36:37], s[0:1], 0x80
	v_and_b32_e32 v126, 63, v0
	v_lshrrev_b32_e32 v128, 6, v0
	v_and_b32_e32 v1, 15, v0
	v_bfe_u32 v24, v0, 4, 2
	v_lshl_or_b32 v107, v128, 4, v1
	v_lshlrev_b32_e32 v106, 2, v107
	v_lshlrev_b32_e32 v127, 2, v0
	v_lshlrev_b32_e32 v25, 1, v107
	v_and_b32_e32 v26, 48, v0
	v_mul_u32_u24_e32 v27, 0x440, v24
	v_lshlrev_b32_e32 v120, 4, v0
	v_lshrrev_b32_e32 v58, 5, v0
	v_mul_u32_u24_e32 v58, 0x110, v58
	v_and_b32_e32 v125, 31, v0
	v_lshl_add_u32 v58, v125, 3, v58
	v_add_u32_e32 v124, 0x1b400, v58
	v_mul_u32_u24_e32 v52, 0x110, v1
	v_add_u32_e32 v52, v52, v26
	v_add_u32_e32 v53, 0x1b400, v52
	v_add_u32_e32 v54, 0x1c500, v52
	v_add_u32_e32 v55, v27, v25
	v_add_u32_e32 v55, 0x1c500, v55
	v_mul_u32_u24_e32 v56, 0x110, v107
	v_add_u32_e32 v56, v56, v26
	v_add_u32_e32 v57, 0x8800, v56
	s_lshl_b32 s12, s2, 4
	s_add_i32 s3, s12, 0xfffff800
	s_cmpk_gt_i32 s2, 0x7f
	s_cselect_b64 s[6:7], -1, 0
	s_mov_b32 s48, 0
	s_mov_b32 s49, -1
	v_lshl_or_b32 v123, s2, 3, v128
	v_lshlrev_b32_e32 v123, 12, v123
	v_lshl_add_u32 v123, v126, 4, v123
	s_waitcnt lgkmcnt(0)
	s_cmpk_lt_i32 s2, 0x80
	s_cselect_b32 s38, s16, s18
	s_cselect_b32 s39, s17, s19
	s_cselect_b32 s40, s20, s24
	s_cselect_b32 s41, s21, s25
	s_cselect_b32 s13, s12, s3
	s_cselect_b32 s44, 0x3db504f3, 1.0
	s_lshl_b32 s13, s13, 9
	s_add_u32 s38, s38, s13
	s_addc_u32 s39, s39, 0
	global_load_dwordx4 v[2:5], v120, s[38:39] nt
	s_and_b32 s13, s2, 7
	s_lshl_b32 s14, s13, 13
	v_add_u32_e32 v125, s14, v120
	global_load_dwordx4 v[80:83], v125, s[40:41]
	s_add_i32 s13, s2, 1
	s_and_b32 s13, s13, 7
	s_lshl_b32 s14, s13, 13
	v_add_u32_e32 v125, s14, v120
	global_load_dwordx4 v[84:87], v125, s[40:41]
	s_add_i32 s13, s2, 2
	s_and_b32 s13, s13, 7
	s_lshl_b32 s14, s13, 13
	v_add_u32_e32 v125, s14, v120
	global_load_dwordx4 v[88:91], v125, s[40:41]
	s_add_i32 s13, s2, 3
	s_and_b32 s13, s13, 7
	s_lshl_b32 s14, s13, 13
	v_add_u32_e32 v125, s14, v120
	global_load_dwordx4 v[92:95], v125, s[40:41]
	s_add_i32 s13, s2, 4
	s_and_b32 s13, s13, 7
	s_lshl_b32 s14, s13, 13
	v_add_u32_e32 v125, s14, v120
	global_load_dwordx4 v[96:99], v125, s[40:41]
	s_add_i32 s13, s2, 5
	s_and_b32 s13, s13, 7
	s_lshl_b32 s14, s13, 13
	v_add_u32_e32 v125, s14, v120
	global_load_dwordx4 v[100:103], v125, s[40:41]
	s_add_i32 s13, s2, 6
	s_and_b32 s13, s13, 7
	s_lshl_b32 s14, s13, 13
	v_add_u32_e32 v125, s14, v120
	global_load_dwordx4 v[108:111], v125, s[40:41]
	s_add_i32 s13, s2, 7
	s_and_b32 s13, s13, 7
	s_lshl_b32 s14, s13, 13
	v_add_u32_e32 v125, s14, v120
	global_load_dwordx4 v[112:115], v125, s[40:41]
	global_load_dword v129, v106, s[32:33]
	global_load_dword v130, v106, s[30:31]
	s_barrier
	s_and_b64 vcc, exec, s[6:7]
	s_cbranch_vccz .Lp_q
	v_cmp_gt_u32_e32 vcc, 32, v126
	v_mov_b32_e32 v198, 0x3db504f3
	v_mov_b32_e32 v125, s22
	v_mov_b32_e32 v104, s26
	v_cndmask_b32_e32 v198, 1.0, v198, vcc
	v_cndmask_b32_e32 v104, v104, v125, vcc
	v_mov_b32_e32 v125, s23
	v_mov_b32_e32 v105, s27
	v_cndmask_b32_e32 v105, v105, v125, vcc
	v_and_b32_e32 v196, 31, v126
	v_lshlrev_b32_e32 v196, 4, v196
	v_mov_b32_e32 v197, 0
	v_lshl_add_u64 v[104:105], v[104:105], 0, v[196:197]
	global_load_dwordx4 v[116:119], v[104:105], off
	v_lshlrev_b32_e32 v121, 14, v128
	v_lshl_add_u32 v121, v126, 4, v121
	s_and_b32 s13, s2, 15
	s_lshl_b32 s14, s13, 10
	s_add_u32 s46, s28, s14
	s_addc_u32 s47, s29, 0
	global_load_dwordx4 v[132:135], v121, s[46:47]
	s_add_i32 s13, s2, 1
	s_and_b32 s13, s13, 15
	s_lshl_b32 s14, s13, 10
	s_add_u32 s46, s28, s14
	s_addc_u32 s47, s29, 0
	global_load_dwordx4 v[136:139], v121, s[46:47]
	s_add_i32 s13, s2, 2
	s_and_b32 s13, s13, 15
	s_lshl_b32 s14, s13, 10
	s_add_u32 s46, s28, s14
	s_addc_u32 s47, s29, 0
	global_load_dwordx4 v[140:143], v121, s[46:47]
	s_add_i32 s13, s2, 3
	s_and_b32 s13, s13, 15
	s_lshl_b32 s14, s13, 10
	s_add_u32 s46, s28, s14
	s_addc_u32 s47, s29, 0
	global_load_dwordx4 v[144:147], v121, s[46:47]
	s_add_i32 s13, s2, 4
	s_and_b32 s13, s13, 15
	s_lshl_b32 s14, s13, 10
	s_add_u32 s46, s28, s14
	s_addc_u32 s47, s29, 0
	global_load_dwordx4 v[148:151], v121, s[46:47]
	s_add_i32 s13, s2, 5
	s_and_b32 s13, s13, 15
	s_lshl_b32 s14, s13, 10
	s_add_u32 s46, s28, s14
	s_addc_u32 s47, s29, 0
	global_load_dwordx4 v[152:155], v121, s[46:47]
	s_add_i32 s13, s2, 6
	s_and_b32 s13, s13, 15
	s_lshl_b32 s14, s13, 10
	s_add_u32 s46, s28, s14
	s_addc_u32 s47, s29, 0
	global_load_dwordx4 v[156:159], v121, s[46:47]
	s_add_i32 s13, s2, 7
	s_and_b32 s13, s13, 15
	s_lshl_b32 s14, s13, 10
	s_add_u32 s46, s28, s14
	s_addc_u32 s47, s29, 0
	global_load_dwordx4 v[160:163], v121, s[46:47]
	s_add_i32 s13, s2, 8
	s_and_b32 s13, s13, 15
	s_lshl_b32 s14, s13, 10
	s_add_u32 s46, s28, s14
	s_addc_u32 s47, s29, 0
	global_load_dwordx4 v[164:167], v121, s[46:47]
	s_add_i32 s13, s2, 9
	s_and_b32 s13, s13, 15
	s_lshl_b32 s14, s13, 10
	s_add_u32 s46, s28, s14
	s_addc_u32 s47, s29, 0
	global_load_dwordx4 v[168:171], v121, s[46:47]
	s_add_i32 s13, s2, 10
	s_and_b32 s13, s13, 15
	s_lshl_b32 s14, s13, 10
	s_add_u32 s46, s28, s14
	s_addc_u32 s47, s29, 0
	global_load_dwordx4 v[172:175], v121, s[46:47]
	s_add_i32 s13, s2, 11
	s_and_b32 s13, s13, 15
	s_lshl_b32 s14, s13, 10
	s_add_u32 s46, s28, s14
	s_addc_u32 s47, s29, 0
	global_load_dwordx4 v[176:179], v121, s[46:47]
	s_add_i32 s13, s2, 12
	s_and_b32 s13, s13, 15
	s_lshl_b32 s14, s13, 10
	s_add_u32 s46, s28, s14
	s_addc_u32 s47, s29, 0
	global_load_dwordx4 v[180:183], v121, s[46:47]
	s_add_i32 s13, s2, 13
	s_and_b32 s13, s13, 15
	s_lshl_b32 s14, s13, 10
	s_add_u32 s46, s28, s14
	s_addc_u32 s47, s29, 0
	global_load_dwordx4 v[184:187], v121, s[46:47]
	s_add_i32 s13, s2, 14
	s_and_b32 s13, s13, 15
	s_lshl_b32 s14, s13, 10
	s_add_u32 s46, s28, s14
	s_addc_u32 s47, s29, 0
	global_load_dwordx4 v[188:191], v121, s[46:47]
	s_add_i32 s13, s2, 15
	s_and_b32 s13, s13, 15
	s_lshl_b32 s14, s13, 10
	s_add_u32 s46, s28, s14
	s_addc_u32 s47, s29, 0
	global_load_dwordx4 v[192:195], v121, s[46:47]
	v_mul_u32_u24_e32 v59, 0x1040, v128
	v_lshl_add_u32 v59, v126, 2, v59
	v_add_u32_e32 v59, 0x11000, v59
	v_mul_u32_u24_e32 v76, 0x1100, v128
	v_lshl_add_u32 v76, v126, 3, v76
	v_add_u32_e32 v76, 0x8700, v76
	v_lshrrev_b32_e32 v77, 2, v126
	v_mul_u32_u24_e32 v77, 0x104, v77
	v_mul_u32_u24_e32 v125, 0x1040, v128
	v_add_u32_e32 v77, v77, v125
	v_and_b32_e32 v125, 3, v126
	v_lshl_add_u32 v77, v125, 6, v77
	v_add_u32_e32 v77, 0x11000, v77
	s_waitcnt vmcnt(27)
	v_cvt_pk_bf16_f32 v12, v2, v3
	v_cvt_pk_bf16_f32 v13, v4, v5
	ds_write_b64 v124, v[12:13]
	s_waitcnt vmcnt(26)
	v_cvt_pk_bf16_f32 v6, v80, v81
	v_cvt_pk_bf16_f32 v7, v82, v83
	s_and_b32 s13, s2, 7
	s_mul_i32 s14, s13, 0x1100
	v_add_u32_e32 v125, s14, v58
	ds_write_b64 v125, v[6:7]
	s_waitcnt vmcnt(25)
	v_cvt_pk_bf16_f32 v8, v84, v85
	v_cvt_pk_bf16_f32 v9, v86, v87
	s_add_i32 s13, s2, 1
	s_and_b32 s13, s13, 7
	s_mul_i32 s14, s13, 0x1100
	v_add_u32_e32 v10, s14, v58
	ds_write_b64 v10, v[8:9]
	s_waitcnt vmcnt(24)
	v_cvt_pk_bf16_f32 v6, v88, v89
	v_cvt_pk_bf16_f32 v7, v90, v91
	s_add_i32 s13, s2, 2
	s_and_b32 s13, s13, 7
	s_mul_i32 s14, s13, 0x1100
	v_add_u32_e32 v125, s14, v58
	ds_write_b64 v125, v[6:7]
	s_waitcnt vmcnt(23)
	v_cvt_pk_bf16_f32 v8, v92, v93
	v_cvt_pk_bf16_f32 v9, v94, v95
	s_add_i32 s13, s2, 3
	s_and_b32 s13, s13, 7
	s_mul_i32 s14, s13, 0x1100
	v_add_u32_e32 v10, s14, v58
	ds_write_b64 v10, v[8:9]
	s_waitcnt vmcnt(22)
	v_cvt_pk_bf16_f32 v6, v96, v97
	v_cvt_pk_bf16_f32 v7, v98, v99
	s_add_i32 s13, s2, 4
	s_and_b32 s13, s13, 7
	s_mul_i32 s14, s13, 0x1100
	v_add_u32_e32 v125, s14, v58
	ds_write_b64 v125, v[6:7]
	s_waitcnt vmcnt(21)
	v_cvt_pk_bf16_f32 v8, v100, v101
	v_cvt_pk_bf16_f32 v9, v102, v103
	s_add_i32 s13, s2, 5
	s_and_b32 s13, s13, 7
	s_mul_i32 s14, s13, 0x1100
	v_add_u32_e32 v10, s14, v58
	ds_write_b64 v10, v[8:9]
	s_waitcnt vmcnt(20)
	v_cvt_pk_bf16_f32 v6, v108, v109
	v_cvt_pk_bf16_f32 v7, v110, v111
	s_add_i32 s13, s2, 6
	s_and_b32 s13, s13, 7
	s_mul_i32 s14, s13, 0x1100
	v_add_u32_e32 v125, s14, v58
	ds_write_b64 v125, v[6:7]
	s_waitcnt vmcnt(19)
	v_cvt_pk_bf16_f32 v8, v112, v113
	v_cvt_pk_bf16_f32 v9, v114, v115
	s_add_i32 s13, s2, 7
	s_and_b32 s13, s13, 7
	s_mul_i32 s14, s13, 0x1100
	v_add_u32_e32 v10, s14, v58
	ds_write_b64 v10, v[8:9]
	s_waitcnt lgkmcnt(0)
	s_barrier
	ds_read_b128 v[28:31], v53
	ds_read_b128 v[60:63], v56
	ds_read_b128 v[32:35], v53 offset:64
	ds_read_b128 v[64:67], v56 offset:64
	ds_read_b128 v[36:39], v53 offset:128
	ds_read_b128 v[68:71], v56 offset:128
	ds_read_b128 v[40:43], v53 offset:192
	ds_read_b128 v[72:75], v56 offset:192
	s_waitcnt lgkmcnt(6)
	v_mfma_f32_16x16x32_bf16 v[18:21], v[28:31], v[60:63], 0
	s_waitcnt lgkmcnt(4)
	v_mfma_f32_16x16x32_bf16 v[18:21], v[32:35], v[64:67], v[18:21]
	s_waitcnt lgkmcnt(2)
	v_mfma_f32_16x16x32_bf16 v[18:21], v[36:39], v[68:71], v[18:21]
	s_waitcnt lgkmcnt(0)
	v_mfma_f32_16x16x32_bf16 v[18:21], v[40:43], v[72:75], v[18:21]
	s_nop 7
	v_mul_f32_e32 v18, s44, v18
	v_mul_f32_e32 v19, s44, v19
	v_mul_f32_e32 v20, s44, v20
	v_mul_f32_e32 v21, s44, v21
	v_cvt_pk_bf16_f32 v18, v18, v18
	v_cvt_pk_bf16_f32 v19, v19, v19
	v_cvt_pk_bf16_f32 v20, v20, v20
	v_cvt_pk_bf16_f32 v21, v21, v21
	ds_write_b16 v55, v18
	ds_write_b16 v55, v19 offset:272
	ds_write_b16 v55, v20 offset:544
	ds_write_b16 v55, v21 offset:816
	s_waitcnt vmcnt(16)
	v_pk_mul_f32 v[116:117], v[198:199], v[116:117] op_sel_hi:[0,1]
	v_pk_mul_f32 v[118:119], v[198:199], v[118:119] op_sel_hi:[0,1]
	s_waitcnt vmcnt(15)
	v_mul_f32_e32 v6, v117, v133
	v_mul_f32_e32 v7, v119, v135
	v_fmac_f32_e32 v6, v116, v132
	v_fmac_f32_e32 v7, v118, v134
	s_and_b32 s13, s2, 15
	s_mul_i32 s14, s13, 0x104
	s_mul_i32 s15, s13, 0x110
	v_add_f32_e32 v6, v6, v7
	v_add_u32_e32 v125, s14, v59
	ds_write_b32 v125, v6
	v_cvt_pk_bf16_f32 v8, v132, v133
	v_cvt_pk_bf16_f32 v9, v134, v135
	v_add_u32_e32 v10, s15, v76
	s_mov_b64 exec, s[48:49]
	ds_write_b64 v10, v[8:9]
	s_mov_b64 exec, -1
	s_waitcnt vmcnt(14)
	v_mul_f32_e32 v11, v117, v137
	v_mul_f32_e32 v15, v119, v139
	v_fmac_f32_e32 v11, v116, v136
	v_fmac_f32_e32 v15, v118, v138
	s_add_i32 s13, s2, 1
	s_and_b32 s13, s13, 15
	s_mul_i32 s14, s13, 0x104
	s_mul_i32 s15, s13, 0x110
	v_add_f32_e32 v11, v11, v15
	v_add_u32_e32 v16, s14, v59
	ds_write_b32 v16, v11
	v_cvt_pk_bf16_f32 v12, v136, v137
	v_cvt_pk_bf16_f32 v13, v138, v139
	v_add_u32_e32 v14, s15, v76
	s_mov_b64 exec, s[48:49]
	ds_write_b64 v14, v[12:13]
	s_mov_b64 exec, -1
	s_waitcnt vmcnt(13)
	v_mul_f32_e32 v6, v117, v141
	v_mul_f32_e32 v7, v119, v143
	v_fmac_f32_e32 v6, v116, v140
	v_fmac_f32_e32 v7, v118, v142
	s_add_i32 s13, s2, 2
	s_and_b32 s13, s13, 15
	s_mul_i32 s14, s13, 0x104
	s_mul_i32 s15, s13, 0x110
	v_add_f32_e32 v6, v6, v7
	v_add_u32_e32 v125, s14, v59
	ds_write_b32 v125, v6
	v_cvt_pk_bf16_f32 v8, v140, v141
	v_cvt_pk_bf16_f32 v9, v142, v143
	v_add_u32_e32 v10, s15, v76
	s_mov_b64 exec, s[48:49]
	ds_write_b64 v10, v[8:9]
	s_mov_b64 exec, -1
	s_waitcnt vmcnt(12)
	v_mul_f32_e32 v11, v117, v145
	v_mul_f32_e32 v15, v119, v147
	v_fmac_f32_e32 v11, v116, v144
	v_fmac_f32_e32 v15, v118, v146
	s_add_i32 s13, s2, 3
	s_and_b32 s13, s13, 15
	s_mul_i32 s14, s13, 0x104
	s_mul_i32 s15, s13, 0x110
	v_add_f32_e32 v11, v11, v15
	v_add_u32_e32 v16, s14, v59
	ds_write_b32 v16, v11
	v_cvt_pk_bf16_f32 v12, v144, v145
	v_cvt_pk_bf16_f32 v13, v146, v147
	v_add_u32_e32 v14, s15, v76
	s_mov_b64 exec, s[48:49]
	ds_write_b64 v14, v[12:13]
	s_mov_b64 exec, -1
	s_waitcnt vmcnt(11)
	v_mul_f32_e32 v6, v117, v149
	v_mul_f32_e32 v7, v119, v151
	v_fmac_f32_e32 v6, v116, v148
	v_fmac_f32_e32 v7, v118, v150
	s_add_i32 s13, s2, 4
	s_and_b32 s13, s13, 15
	s_mul_i32 s14, s13, 0x104
	s_mul_i32 s15, s13, 0x110
	v_add_f32_e32 v6, v6, v7
	v_add_u32_e32 v125, s14, v59
	ds_write_b32 v125, v6
	v_cvt_pk_bf16_f32 v8, v148, v149
	v_cvt_pk_bf16_f32 v9, v150, v151
	v_add_u32_e32 v10, s15, v76
	s_mov_b64 exec, s[48:49]
	ds_write_b64 v10, v[8:9]
	s_mov_b64 exec, -1
	s_waitcnt vmcnt(10)
	v_mul_f32_e32 v11, v117, v153
	v_mul_f32_e32 v15, v119, v155
	v_fmac_f32_e32 v11, v116, v152
	v_fmac_f32_e32 v15, v118, v154
	s_add_i32 s13, s2, 5
	s_and_b32 s13, s13, 15
	s_mul_i32 s14, s13, 0x104
	s_mul_i32 s15, s13, 0x110
	v_add_f32_e32 v11, v11, v15
	v_add_u32_e32 v16, s14, v59
	ds_write_b32 v16, v11
	v_cvt_pk_bf16_f32 v12, v152, v153
	v_cvt_pk_bf16_f32 v13, v154, v155
	v_add_u32_e32 v14, s15, v76
	s_mov_b64 exec, s[48:49]
	ds_write_b64 v14, v[12:13]
	s_mov_b64 exec, -1
	s_waitcnt vmcnt(9)
	v_mul_f32_e32 v6, v117, v157
	v_mul_f32_e32 v7, v119, v159
	v_fmac_f32_e32 v6, v116, v156
	v_fmac_f32_e32 v7, v118, v158
	s_add_i32 s13, s2, 6
	s_and_b32 s13, s13, 15
	s_mul_i32 s14, s13, 0x104
	s_mul_i32 s15, s13, 0x110
	v_add_f32_e32 v6, v6, v7
	v_add_u32_e32 v125, s14, v59
	ds_write_b32 v125, v6
	v_cvt_pk_bf16_f32 v8, v156, v157
	v_cvt_pk_bf16_f32 v9, v158, v159
	v_add_u32_e32 v10, s15, v76
	s_mov_b64 exec, s[48:49]
	ds_write_b64 v10, v[8:9]
	s_mov_b64 exec, -1
	s_waitcnt vmcnt(8)
	v_mul_f32_e32 v11, v117, v161
	v_mul_f32_e32 v15, v119, v163
	v_fmac_f32_e32 v11, v116, v160
	v_fmac_f32_e32 v15, v118, v162
	s_add_i32 s13, s2, 7
	s_and_b32 s13, s13, 15
	s_mul_i32 s14, s13, 0x104
	s_mul_i32 s15, s13, 0x110
	v_add_f32_e32 v11, v11, v15
	v_add_u32_e32 v16, s14, v59
	ds_write_b32 v16, v11
	v_cvt_pk_bf16_f32 v12, v160, v161
	v_cvt_pk_bf16_f32 v13, v162, v163
	v_add_u32_e32 v14, s15, v76
	s_mov_b64 exec, s[48:49]
	ds_write_b64 v14, v[12:13]
	s_mov_b64 exec, -1
	s_waitcnt vmcnt(7)
	v_mul_f32_e32 v6, v117, v165
	v_mul_f32_e32 v7, v119, v167
	v_fmac_f32_e32 v6, v116, v164
	v_fmac_f32_e32 v7, v118, v166
	s_add_i32 s13, s2, 8
	s_and_b32 s13, s13, 15
	s_mul_i32 s14, s13, 0x104
	s_mul_i32 s15, s13, 0x110
	v_add_f32_e32 v6, v6, v7
	v_add_u32_e32 v125, s14, v59
	ds_write_b32 v125, v6
	v_cvt_pk_bf16_f32 v8, v164, v165
	v_cvt_pk_bf16_f32 v9, v166, v167
	v_add_u32_e32 v10, s15, v76
	s_mov_b64 exec, s[48:49]
	ds_write_b64 v10, v[8:9]
	s_mov_b64 exec, -1
	s_waitcnt vmcnt(6)
	v_mul_f32_e32 v11, v117, v169
	v_mul_f32_e32 v15, v119, v171
	v_fmac_f32_e32 v11, v116, v168
	v_fmac_f32_e32 v15, v118, v170
	s_add_i32 s13, s2, 9
	s_and_b32 s13, s13, 15
	s_mul_i32 s14, s13, 0x104
	s_mul_i32 s15, s13, 0x110
	v_add_f32_e32 v11, v11, v15
	v_add_u32_e32 v16, s14, v59
	ds_write_b32 v16, v11
	v_cvt_pk_bf16_f32 v12, v168, v169
	v_cvt_pk_bf16_f32 v13, v170, v171
	v_add_u32_e32 v14, s15, v76
	s_mov_b64 exec, s[48:49]
	ds_write_b64 v14, v[12:13]
	s_mov_b64 exec, -1
	s_waitcnt vmcnt(5)
	v_mul_f32_e32 v6, v117, v173
	v_mul_f32_e32 v7, v119, v175
	v_fmac_f32_e32 v6, v116, v172
	v_fmac_f32_e32 v7, v118, v174
	s_add_i32 s13, s2, 10
	s_and_b32 s13, s13, 15
	s_mul_i32 s14, s13, 0x104
	s_mul_i32 s15, s13, 0x110
	v_add_f32_e32 v6, v6, v7
	v_add_u32_e32 v125, s14, v59
	ds_write_b32 v125, v6
	v_cvt_pk_bf16_f32 v8, v172, v173
	v_cvt_pk_bf16_f32 v9, v174, v175
	v_add_u32_e32 v10, s15, v76
	s_mov_b64 exec, s[48:49]
	ds_write_b64 v10, v[8:9]
	s_mov_b64 exec, -1
	s_waitcnt vmcnt(4)
	v_mul_f32_e32 v11, v117, v177
	v_mul_f32_e32 v15, v119, v179
	v_fmac_f32_e32 v11, v116, v176
	v_fmac_f32_e32 v15, v118, v178
	s_add_i32 s13, s2, 11
	s_and_b32 s13, s13, 15
	s_mul_i32 s14, s13, 0x104
	s_mul_i32 s15, s13, 0x110
	v_add_f32_e32 v11, v11, v15
	v_add_u32_e32 v16, s14, v59
	ds_write_b32 v16, v11
	v_cvt_pk_bf16_f32 v12, v176, v177
	v_cvt_pk_bf16_f32 v13, v178, v179
	v_add_u32_e32 v14, s15, v76
	s_mov_b64 exec, s[48:49]
	ds_write_b64 v14, v[12:13]
	s_mov_b64 exec, -1
	s_waitcnt vmcnt(3)
	v_mul_f32_e32 v6, v117, v181
	v_mul_f32_e32 v7, v119, v183
	v_fmac_f32_e32 v6, v116, v180
	v_fmac_f32_e32 v7, v118, v182
	s_add_i32 s13, s2, 12
	s_and_b32 s13, s13, 15
	s_mul_i32 s14, s13, 0x104
	s_mul_i32 s15, s13, 0x110
	v_add_f32_e32 v6, v6, v7
	v_add_u32_e32 v125, s14, v59
	ds_write_b32 v125, v6
	v_cvt_pk_bf16_f32 v8, v180, v181
	v_cvt_pk_bf16_f32 v9, v182, v183
	v_add_u32_e32 v10, s15, v76
	s_mov_b64 exec, s[48:49]
	ds_write_b64 v10, v[8:9]
	s_mov_b64 exec, -1
	s_waitcnt vmcnt(2)
	v_mul_f32_e32 v11, v117, v185
	v_mul_f32_e32 v15, v119, v187
	v_fmac_f32_e32 v11, v116, v184
	v_fmac_f32_e32 v15, v118, v186
	s_add_i32 s13, s2, 13
	s_and_b32 s13, s13, 15
	s_mul_i32 s14, s13, 0x104
	s_mul_i32 s15, s13, 0x110
	v_add_f32_e32 v11, v11, v15
	v_add_u32_e32 v16, s14, v59
	ds_write_b32 v16, v11
	v_cvt_pk_bf16_f32 v12, v184, v185
	v_cvt_pk_bf16_f32 v13, v186, v187
	v_add_u32_e32 v14, s15, v76
	s_mov_b64 exec, s[48:49]
	ds_write_b64 v14, v[12:13]
	s_mov_b64 exec, -1
	s_waitcnt vmcnt(1)
	v_mul_f32_e32 v6, v117, v189
	v_mul_f32_e32 v7, v119, v191
	v_fmac_f32_e32 v6, v116, v188
	v_fmac_f32_e32 v7, v118, v190
	s_add_i32 s13, s2, 14
	s_and_b32 s13, s13, 15
	s_mul_i32 s14, s13, 0x104
	s_mul_i32 s15, s13, 0x110
	v_add_f32_e32 v6, v6, v7
	v_add_u32_e32 v125, s14, v59
	ds_write_b32 v125, v6
	v_cvt_pk_bf16_f32 v8, v188, v189
	v_cvt_pk_bf16_f32 v9, v190, v191
	v_add_u32_e32 v10, s15, v76
	s_mov_b64 exec, s[48:49]
	ds_write_b64 v10, v[8:9]
	s_mov_b64 exec, -1
	s_waitcnt vmcnt(0)
	v_mul_f32_e32 v11, v117, v193
	v_mul_f32_e32 v15, v119, v195
	v_fmac_f32_e32 v11, v116, v192
	v_fmac_f32_e32 v15, v118, v194
	s_add_i32 s13, s2, 15
	s_and_b32 s13, s13, 15
	s_mul_i32 s14, s13, 0x104
	s_mul_i32 s15, s13, 0x110
	v_add_f32_e32 v11, v11, v15
	v_add_u32_e32 v16, s14, v59
	ds_write_b32 v16, v11
	v_cvt_pk_bf16_f32 v12, v192, v193
	v_cvt_pk_bf16_f32 v13, v194, v195
	v_add_u32_e32 v14, s15, v76
	s_mov_b64 exec, s[48:49]
	ds_write_b64 v14, v[12:13]
	s_mov_b64 exec, -1
	s_waitcnt lgkmcnt(0)
	ds_read2_b32 v[60:61], v77 offset0:0 offset1:1
	ds_read2_b32 v[62:63], v77 offset0:2 offset1:3
	ds_read2_b32 v[64:65], v77 offset0:4 offset1:5
	ds_read2_b32 v[66:67], v77 offset0:6 offset1:7
	ds_read2_b32 v[68:69], v77 offset0:8 offset1:9
	ds_read2_b32 v[70:71], v77 offset0:10 offset1:11
	ds_read2_b32 v[72:73], v77 offset0:12 offset1:13
	ds_read2_b32 v[74:75], v77 offset0:14 offset1:15
	s_waitcnt lgkmcnt(0)
	v_add_f32_e32 v78, 0, v60
	v_add_f32_e32 v78, v78, v61
	v_add_f32_e32 v78, v78, v62
	v_add_f32_e32 v78, v78, v63
	v_add_f32_e32 v78, v78, v64
	v_add_f32_e32 v78, v78, v65
	v_add_f32_e32 v78, v78, v66
	v_add_f32_e32 v78, v78, v67
	v_add_f32_e32 v78, v78, v68
	v_add_f32_e32 v78, v78, v69
	v_add_f32_e32 v78, v78, v70
	v_add_f32_e32 v78, v78, v71
	v_add_f32_e32 v78, v78, v72
	v_add_f32_e32 v78, v78, v73
	v_add_f32_e32 v78, v78, v74
	v_add_f32_e32 v78, v78, v75
	s_nop 1
	v_add_f32_dpp v78, v78, v78 quad_perm:[1,0,3,2] row_mask:0xf bank_mask:0xf bound_ctrl:1
	s_nop 1
	v_add_f32_dpp v78, v78, v78 quad_perm:[2,3,0,1] row_mask:0xf bank_mask:0xf bound_ctrl:1
	v_lshlrev_b32_e32 v79, 4, v1
	ds_bpermute_b32 v78, v79, v78
	s_waitcnt lgkmcnt(0)
	s_barrier
	global_load_dwordx4 v[2:5], v123, s[34:35] nt
	global_load_dwordx4 v[6:9], v123, s[34:35] offset:1024 nt
	global_load_dwordx4 v[10:13], v123, s[34:35] offset:2048 nt
	global_load_dwordx4 v[14:17], v123, s[34:35] offset:3072 nt
	ds_read_b128 v[28:31], v54
	ds_read_b128 v[60:63], v57
	ds_read_b128 v[32:35], v54 offset:64
	ds_read_b128 v[64:67], v57 offset:64
	ds_read_b128 v[36:39], v54 offset:128
	ds_read_b128 v[68:71], v57 offset:128
	ds_read_b128 v[40:43], v54 offset:192
	ds_read_b128 v[72:75], v57 offset:192
	s_waitcnt lgkmcnt(6)
	v_mfma_f32_16x16x32_bf16 v[18:21], v[28:31], v[60:63], 0
	s_waitcnt lgkmcnt(4)
	v_mfma_f32_16x16x32_bf16 v[18:21], v[32:35], v[64:67], v[18:21]
	s_waitcnt lgkmcnt(2)
	v_mfma_f32_16x16x32_bf16 v[18:21], v[36:39], v[68:71], v[18:21]
	s_waitcnt lgkmcnt(0)
	v_mfma_f32_16x16x32_bf16 v[18:21], v[40:43], v[72:75], v[18:21]
	s_nop 2
	v_mov_b32_e32 v28, v78
	s_load_dwordx2 s[4:5], s[0:1], 0x70
	v_lshl_or_b32 v30, v24, 2, s3
	v_ashrrev_i32_e32 v31, 31, v30
	v_mov_b32_e32 v107, 0
	s_waitcnt lgkmcnt(0)
	v_add_f32_e32 v34, v130, v28
	v_add_f32_e32 v35, v34, v18
	v_add_f32_e32 v28, v35, v35
	v_mul_f32_e32 v28, 0x3fb8aa3b, v28
	v_exp_f32_e32 v32, v28
	v_lshlrev_b64 v[28:29], 9, v[30:31]
	s_mov_b32 s8, 0x19200
	v_add3_u32 v37, v27, v25, s8
	v_add_f32_e32 v31, 1.0, v32
	v_rcp_f32_e32 v31, v31
	v_lshl_add_u64 v[32:33], s[4:5], 0, v[106:107]
	v_lshl_add_u64 v[28:29], v[32:33], 0, v[28:29]
	global_store_dword v[28:29], v35, off sc1
	v_fma_f32 v35, v31, -2.0, 1.0
	v_fma_f32 v28, -v35, v35, 1.0
	v_mul_f32_e32 v28, v129, v28
	v_add_f32_e32 v31, v34, v19
	v_cvt_pk_bf16_f32 v29, v28, s0
	v_mul_f32_e64 v27, v35, -v28
	v_add_f32_e32 v28, v31, v31
	v_mul_f32_e32 v28, 0x3fb8aa3b, v28
	v_exp_f32_e32 v38, v28
	v_cvt_pk_bf16_f32 v27, v27, s0
	ds_write_b16 v37, v27 offset:4352
	v_or_b32_e32 v28, 1, v30
	v_add_f32_e32 v27, 1.0, v38
	v_rcp_f32_e32 v27, v27
	ds_write_b16 v37, v29
	v_ashrrev_i32_e32 v29, 31, v28
	v_lshlrev_b64 v[28:29], 9, v[28:29]
	v_lshl_add_u64 v[28:29], v[32:33], 0, v[28:29]
	v_fma_f32 v27, v27, -2.0, 1.0
	global_store_dword v[28:29], v31, off sc1
	v_fma_f32 v28, -v27, v27, 1.0
	v_mul_f32_e32 v28, v129, v28
	v_cvt_pk_bf16_f32 v29, v28, s0
	v_add_f32_e32 v31, v34, v20
	ds_write_b16 v37, v29 offset:272
	v_add_f32_e32 v29, v31, v31
	v_mul_f32_e32 v29, 0x3fb8aa3b, v29
	v_exp_f32_e32 v38, v29
	v_mul_f32_e64 v28, v27, -v28
	v_cvt_pk_bf16_f32 v28, v28, s0
	ds_write_b16 v37, v28 offset:4624
	v_add_f32_e32 v38, 1.0, v38
	v_or_b32_e32 v28, 2, v30
	v_rcp_f32_e32 v38, v38
	v_ashrrev_i32_e32 v29, 31, v28
	v_lshlrev_b64 v[28:29], 9, v[28:29]
	v_lshl_add_u64 v[28:29], v[32:33], 0, v[28:29]
	global_store_dword v[28:29], v31, off sc1
	v_fma_f32 v28, v38, -2.0, 1.0
	v_fma_f32 v29, -v28, v28, 1.0
	v_mul_f32_e32 v29, v129, v29
	v_cvt_pk_bf16_f32 v31, v29, s0
	v_add_f32_e32 v34, v34, v21
	ds_write_b16 v37, v31 offset:544
	v_add_f32_e32 v31, v34, v34
	v_mul_f32_e32 v31, 0x3fb8aa3b, v31
	v_exp_f32_e32 v38, v31
	v_mul_f32_e64 v29, v28, -v29
	v_cvt_pk_bf16_f32 v29, v29, s0
	ds_write_b16 v37, v29 offset:4896
	v_add_f32_e32 v29, 1.0, v38
	v_rcp_f32_e32 v29, v29
	v_or_b32_e32 v30, 3, v30
	v_ashrrev_i32_e32 v31, 31, v30
	v_lshlrev_b64 v[30:31], 9, v[30:31]
	v_lshl_add_u64 v[30:31], v[32:33], 0, v[30:31]
	v_fma_f32 v29, v29, -2.0, 1.0
	global_store_dword v[30:31], v34, off sc1
	v_fma_f32 v30, -v29, v29, 1.0
	v_mul_f32_e32 v30, v129, v30
	v_cvt_pk_bf16_f32 v31, v30, s0
	v_mul_f32_e64 v30, v29, -v30
	v_cvt_pk_bf16_f32 v30, v30, s0
	ds_write_b16 v37, v30 offset:5168
	v_mov_b32_e32 v30, 0x1d800
	v_mul_f32_e32 v36, v129, v35
	v_lshl_or_b32 v32, v128, 6, v30
	v_mov_b32_e32 v30, v107
	ds_write_b16 v37, v31 offset:816
	v_mov_b32_e32 v31, 0
	v_mov_b32_dpp v30, v36 quad_perm:[1,0,3,2] row_mask:0xf bank_mask:0xf
	v_fmac_f32_e32 v30, v129, v35
	v_cmp_eq_u32_e32 vcc, 0, v1
	v_add_u32_e32 v26, v32, v26
	v_add_f32_dpp v30, v30, v30 quad_perm:[2,3,0,1] row_mask:0xf bank_mask:0xf bound_ctrl:1
	s_nop 1
	v_add_f32_dpp v30, v30, v30 row_half_mirror row_mask:0xf bank_mask:0xf bound_ctrl:1
	s_nop 1
	v_mov_b32_dpp v31, v30 row_mirror row_mask:0xf bank_mask:0xf
	s_and_saveexec_b64 s[4:5], vcc
	v_add_f32_e32 v30, v30, v31
	ds_write_b32 v26, v30
	s_or_b64 exec, exec, s[4:5]
	v_mul_f32_e32 v30, v129, v27
	v_mov_b32_e32 v31, 0
	s_nop 1
	v_mov_b32_dpp v31, v30 quad_perm:[1,0,3,2] row_mask:0xf bank_mask:0xf
	v_fmac_f32_e32 v31, v129, v27
	s_nop 1
	v_add_f32_dpp v27, v31, v31 quad_perm:[2,3,0,1] row_mask:0xf bank_mask:0xf bound_ctrl:1
	s_nop 1
	v_add_f32_dpp v27, v27, v27 row_half_mirror row_mask:0xf bank_mask:0xf bound_ctrl:1
	s_nop 1
	v_mov_b32_dpp v107, v27 row_mirror row_mask:0xf bank_mask:0xf
	s_and_saveexec_b64 s[4:5], vcc
	v_add_f32_e32 v27, v27, v107
	ds_write_b32 v26, v27 offset:4
	s_or_b64 exec, exec, s[4:5]
	v_mul_f32_e32 v30, v129, v28
	v_mov_b32_e32 v31, 0
	v_mov_b32_e32 v27, 0
	s_nop 0
	v_mov_b32_dpp v31, v30 quad_perm:[1,0,3,2] row_mask:0xf bank_mask:0xf
	v_fmac_f32_e32 v31, v129, v28
	v_mov_b32_e32 v30, 0
	s_nop 0
	v_add_f32_dpp v28, v31, v31 quad_perm:[2,3,0,1] row_mask:0xf bank_mask:0xf bound_ctrl:1
	s_nop 1
	v_add_f32_dpp v28, v28, v28 row_half_mirror row_mask:0xf bank_mask:0xf bound_ctrl:1
	s_nop 1
	v_mov_b32_dpp v30, v28 row_mirror row_mask:0xf bank_mask:0xf
	s_and_saveexec_b64 s[4:5], vcc
	v_add_f32_e32 v28, v28, v30
	ds_write_b32 v26, v28 offset:8
	s_or_b64 exec, exec, s[4:5]
	v_mul_f32_e32 v28, v129, v29
	v_mov_b32_e32 v30, 0
	s_nop 1
	v_mov_b32_dpp v30, v28 quad_perm:[1,0,3,2] row_mask:0xf bank_mask:0xf
	v_fmac_f32_e32 v30, v129, v29
	s_nop 1
	v_add_f32_dpp v28, v30, v30 quad_perm:[2,3,0,1] row_mask:0xf bank_mask:0xf bound_ctrl:1
	s_nop 1
	v_add_f32_dpp v28, v28, v28 row_half_mirror row_mask:0xf bank_mask:0xf bound_ctrl:1
	s_nop 1
	v_mov_b32_dpp v27, v28 row_mirror row_mask:0xf bank_mask:0xf
	s_and_saveexec_b64 s[4:5], vcc
	v_add_f32_e32 v27, v28, v27
	ds_write_b32 v26, v27 offset:12
	s_or_b64 exec, exec, s[4:5]
	s_mov_b64 s[4:5], 0
	s_branch .LBB0_28
.Lp_q:
	v_lshrrev_b32_e32 v122, 5, v0
	v_lshlrev_b32_e32 v122, 10, v122
	v_and_b32_e32 v125, 31, v0
	v_lshl_add_u32 v122, v125, 4, v122
	s_and_b32 s13, s2, 7
	s_lshl_b32 s14, s13, 14
	v_add_u32_e32 v125, s14, v122
	global_load_dwordx4 v[132:135], v125, s[28:29]
	s_add_i32 s13, s2, 1
	s_and_b32 s13, s13, 7
	s_lshl_b32 s14, s13, 14
	v_add_u32_e32 v125, s14, v122
	global_load_dwordx4 v[136:139], v125, s[28:29]
	s_add_i32 s13, s2, 2
	s_and_b32 s13, s13, 7
	s_lshl_b32 s14, s13, 14
	v_add_u32_e32 v125, s14, v122
	global_load_dwordx4 v[140:143], v125, s[28:29]
	s_add_i32 s13, s2, 3
	s_and_b32 s13, s13, 7
	s_lshl_b32 s14, s13, 14
	v_add_u32_e32 v125, s14, v122
	global_load_dwordx4 v[144:147], v125, s[28:29]
	s_add_i32 s13, s2, 4
	s_and_b32 s13, s13, 7
	s_lshl_b32 s14, s13, 14
	v_add_u32_e32 v125, s14, v122
	global_load_dwordx4 v[148:151], v125, s[28:29]
	s_add_i32 s13, s2, 5
	s_and_b32 s13, s13, 7
	s_lshl_b32 s14, s13, 14
	v_add_u32_e32 v125, s14, v122
	global_load_dwordx4 v[152:155], v125, s[28:29]
	s_add_i32 s13, s2, 6
	s_and_b32 s13, s13, 7
	s_lshl_b32 s14, s13, 14
	v_add_u32_e32 v125, s14, v122
	global_load_dwordx4 v[156:159], v125, s[28:29]
	s_add_i32 s13, s2, 7
	s_and_b32 s13, s13, 7
	s_lshl_b32 s14, s13, 14
	v_add_u32_e32 v125, s14, v122
	global_load_dwordx4 v[160:163], v125, s[28:29]
	s_waitcnt vmcnt(18)
	v_cvt_pk_bf16_f32 v12, v2, v3
	v_cvt_pk_bf16_f32 v13, v4, v5
	ds_write_b64 v124, v[12:13]
	s_waitcnt vmcnt(17)
	v_cvt_pk_bf16_f32 v6, v80, v81
	v_cvt_pk_bf16_f32 v7, v82, v83
	s_and_b32 s13, s2, 7
	s_mul_i32 s14, s13, 0x1100
	v_add_u32_e32 v125, s14, v58
	ds_write_b64 v125, v[6:7]
	s_waitcnt vmcnt(16)
	v_cvt_pk_bf16_f32 v8, v84, v85
	v_cvt_pk_bf16_f32 v9, v86, v87
	s_add_i32 s13, s2, 1
	s_and_b32 s13, s13, 7
	s_mul_i32 s14, s13, 0x1100
	v_add_u32_e32 v10, s14, v58
	ds_write_b64 v10, v[8:9]
	s_waitcnt vmcnt(15)
	v_cvt_pk_bf16_f32 v6, v88, v89
	v_cvt_pk_bf16_f32 v7, v90, v91
	s_add_i32 s13, s2, 2
	s_and_b32 s13, s13, 7
	s_mul_i32 s14, s13, 0x1100
	v_add_u32_e32 v125, s14, v58
	ds_write_b64 v125, v[6:7]
	s_waitcnt vmcnt(14)
	v_cvt_pk_bf16_f32 v8, v92, v93
	v_cvt_pk_bf16_f32 v9, v94, v95
	s_add_i32 s13, s2, 3
	s_and_b32 s13, s13, 7
	s_mul_i32 s14, s13, 0x1100
	v_add_u32_e32 v10, s14, v58
	ds_write_b64 v10, v[8:9]
	s_waitcnt vmcnt(13)
	v_cvt_pk_bf16_f32 v6, v96, v97
	v_cvt_pk_bf16_f32 v7, v98, v99
	s_add_i32 s13, s2, 4
	s_and_b32 s13, s13, 7
	s_mul_i32 s14, s13, 0x1100
	v_add_u32_e32 v125, s14, v58
	ds_write_b64 v125, v[6:7]
	s_waitcnt vmcnt(12)
	v_cvt_pk_bf16_f32 v8, v100, v101
	v_cvt_pk_bf16_f32 v9, v102, v103
	s_add_i32 s13, s2, 5
	s_and_b32 s13, s13, 7
	s_mul_i32 s14, s13, 0x1100
	v_add_u32_e32 v10, s14, v58
	ds_write_b64 v10, v[8:9]
	s_waitcnt vmcnt(11)
	v_cvt_pk_bf16_f32 v6, v108, v109
	v_cvt_pk_bf16_f32 v7, v110, v111
	s_add_i32 s13, s2, 6
	s_and_b32 s13, s13, 7
	s_mul_i32 s14, s13, 0x1100
	v_add_u32_e32 v125, s14, v58
	ds_write_b64 v125, v[6:7]
	s_waitcnt vmcnt(10)
	v_cvt_pk_bf16_f32 v8, v112, v113
	v_cvt_pk_bf16_f32 v9, v114, v115
	s_add_i32 s13, s2, 7
	s_and_b32 s13, s13, 7
	s_mul_i32 s14, s13, 0x1100
	v_add_u32_e32 v10, s14, v58
	ds_write_b64 v10, v[8:9]
	s_waitcnt lgkmcnt(0)
	s_barrier
	ds_read_b128 v[28:31], v53
	ds_read_b128 v[60:63], v56
	ds_read_b128 v[32:35], v53 offset:64
	ds_read_b128 v[64:67], v56 offset:64
	ds_read_b128 v[36:39], v53 offset:128
	ds_read_b128 v[68:71], v56 offset:128
	ds_read_b128 v[40:43], v53 offset:192
	ds_read_b128 v[72:75], v56 offset:192
	s_waitcnt lgkmcnt(6)
	v_mfma_f32_16x16x32_bf16 v[18:21], v[28:31], v[60:63], 0
	s_waitcnt lgkmcnt(4)
	v_mfma_f32_16x16x32_bf16 v[18:21], v[32:35], v[64:67], v[18:21]
	s_waitcnt lgkmcnt(2)
	v_mfma_f32_16x16x32_bf16 v[18:21], v[36:39], v[68:71], v[18:21]
	s_waitcnt lgkmcnt(0)
	v_mfma_f32_16x16x32_bf16 v[18:21], v[40:43], v[72:75], v[18:21]
	s_nop 7
	v_mul_f32_e32 v18, s44, v18
	v_mul_f32_e32 v19, s44, v19
	v_mul_f32_e32 v20, s44, v20
	v_mul_f32_e32 v21, s44, v21
	v_cvt_pk_bf16_f32 v18, v18, v18
	v_cvt_pk_bf16_f32 v19, v19, v19
	v_cvt_pk_bf16_f32 v20, v20, v20
	v_cvt_pk_bf16_f32 v21, v21, v21
	ds_write_b16 v55, v18
	ds_write_b16 v55, v19 offset:272
	ds_write_b16 v55, v20 offset:544
	ds_write_b16 v55, v21 offset:816
	s_waitcnt vmcnt(7)
	v_cvt_pk_bf16_f32 v6, v132, v133
	v_cvt_pk_bf16_f32 v7, v134, v135
	s_and_b32 s13, s2, 7
	s_mul_i32 s14, s13, 0x1100
	s_add_i32 s14, s14, 34816
	v_add_u32_e32 v125, s14, v58
	ds_write_b64 v125, v[6:7]
	s_waitcnt vmcnt(6)
	v_cvt_pk_bf16_f32 v8, v136, v137
	v_cvt_pk_bf16_f32 v9, v138, v139
	s_add_i32 s13, s2, 1
	s_and_b32 s13, s13, 7
	s_mul_i32 s14, s13, 0x1100
	s_add_i32 s14, s14, 34816
	v_add_u32_e32 v10, s14, v58
	ds_write_b64 v10, v[8:9]
	s_waitcnt vmcnt(5)
	v_cvt_pk_bf16_f32 v6, v140, v141
	v_cvt_pk_bf16_f32 v7, v142, v143
	s_add_i32 s13, s2, 2
	s_and_b32 s13, s13, 7
	s_mul_i32 s14, s13, 0x1100
	s_add_i32 s14, s14, 34816
	v_add_u32_e32 v125, s14, v58
	ds_write_b64 v125, v[6:7]
	s_waitcnt vmcnt(4)
	v_cvt_pk_bf16_f32 v8, v144, v145
	v_cvt_pk_bf16_f32 v9, v146, v147
	s_add_i32 s13, s2, 3
	s_and_b32 s13, s13, 7
	s_mul_i32 s14, s13, 0x1100
	s_add_i32 s14, s14, 34816
	v_add_u32_e32 v10, s14, v58
	ds_write_b64 v10, v[8:9]
	s_waitcnt vmcnt(3)
	v_cvt_pk_bf16_f32 v6, v148, v149
	v_cvt_pk_bf16_f32 v7, v150, v151
	s_add_i32 s13, s2, 4
	s_and_b32 s13, s13, 7
	s_mul_i32 s14, s13, 0x1100
	s_add_i32 s14, s14, 34816
	v_add_u32_e32 v125, s14, v58
	ds_write_b64 v125, v[6:7]
	s_waitcnt vmcnt(2)
	v_cvt_pk_bf16_f32 v8, v152, v153
	v_cvt_pk_bf16_f32 v9, v154, v155
	s_add_i32 s13, s2, 5
	s_and_b32 s13, s13, 7
	s_mul_i32 s14, s13, 0x1100
	s_add_i32 s14, s14, 34816
	v_add_u32_e32 v10, s14, v58
	ds_write_b64 v10, v[8:9]
	s_waitcnt vmcnt(1)
	v_cvt_pk_bf16_f32 v6, v156, v157
	v_cvt_pk_bf16_f32 v7, v158, v159
	s_add_i32 s13, s2, 6
	s_and_b32 s13, s13, 7
	s_mul_i32 s14, s13, 0x1100
	s_add_i32 s14, s14, 34816
	v_add_u32_e32 v125, s14, v58
	ds_write_b64 v125, v[6:7]
	s_waitcnt vmcnt(0)
	v_cvt_pk_bf16_f32 v8, v160, v161
	v_cvt_pk_bf16_f32 v9, v162, v163
	s_add_i32 s13, s2, 7
	s_and_b32 s13, s13, 7
	s_mul_i32 s14, s13, 0x1100
	s_add_i32 s14, s14, 34816
	v_add_u32_e32 v10, s14, v58
	ds_write_b64 v10, v[8:9]
	s_waitcnt lgkmcnt(0)
	s_barrier
	global_load_dwordx4 v[2:5], v123, s[34:35] nt
	global_load_dwordx4 v[6:9], v123, s[34:35] offset:1024 nt
	global_load_dwordx4 v[10:13], v123, s[34:35] offset:2048 nt
	global_load_dwordx4 v[14:17], v123, s[34:35] offset:3072 nt
	ds_read_b128 v[28:31], v54
	ds_read_b128 v[60:63], v57
	ds_read_b128 v[32:35], v54 offset:64
	ds_read_b128 v[64:67], v57 offset:64
	ds_read_b128 v[36:39], v54 offset:128
	ds_read_b128 v[68:71], v57 offset:128
	ds_read_b128 v[40:43], v54 offset:192
	ds_read_b128 v[72:75], v57 offset:192
	s_waitcnt lgkmcnt(6)
	v_mfma_f32_16x16x32_bf16 v[18:21], v[28:31], v[60:63], 0
	s_waitcnt lgkmcnt(4)
	v_mfma_f32_16x16x32_bf16 v[18:21], v[32:35], v[64:67], v[18:21]
	s_waitcnt lgkmcnt(2)
	v_mfma_f32_16x16x32_bf16 v[18:21], v[36:39], v[68:71], v[18:21]
	s_waitcnt lgkmcnt(0)
	v_mfma_f32_16x16x32_bf16 v[18:21], v[40:43], v[72:75], v[18:21]
	s_load_dwordx2 s[4:5], s[0:1], 0x68
	v_lshl_or_b32 v26, v24, 2, s12
	v_mov_b32_e32 v107, 0
	v_ashrrev_i32_e32 v27, 31, v26
	v_lshlrev_b64 v[28:29], 9, v[26:27]
	s_waitcnt lgkmcnt(0)
	v_lshl_add_u64 v[30:31], s[4:5], 0, v[106:107]
	v_lshl_add_u64 v[28:29], v[30:31], 0, v[28:29]
	v_mul_u32_u24_e32 v24, 0x440, v24
	s_mov_b32 s4, 0x19200
	global_store_dword v[28:29], v18, off sc1
	v_add3_u32 v28, v24, v25, s4
	v_mul_f32_e32 v24, v18, v18
	v_cvt_pk_bf16_f32 v27, v18, s0
	v_cvt_pk_bf16_f32 v24, v24, s0
	ds_write_b16 v28, v27
	ds_write_b16 v28, v24 offset:4352
	v_max3_f32 v27, |v18|, 0, |v19|
	v_or_b32_e32 v24, 1, v26
	v_cvt_pk_bf16_f32 v18, v19, s0
	v_ashrrev_i32_e32 v25, 31, v24
	ds_write_b16 v28, v18 offset:272
	v_mul_f32_e32 v18, v19, v19
	v_lshlrev_b64 v[24:25], 9, v[24:25]
	v_cvt_pk_bf16_f32 v18, v18, s0
	v_lshl_add_u64 v[24:25], v[30:31], 0, v[24:25]
	ds_write_b16 v28, v18 offset:4624
	v_or_b32_e32 v18, 2, v26
	global_store_dword v[24:25], v19, off sc1
	v_ashrrev_i32_e32 v19, 31, v18
	v_lshlrev_b64 v[18:19], 9, v[18:19]
	v_lshl_add_u64 v[18:19], v[30:31], 0, v[18:19]
	global_store_dword v[18:19], v20, off sc1
	v_cvt_pk_bf16_f32 v18, v20, s0
	ds_write_b16 v28, v18 offset:544
	v_mul_f32_e32 v18, v20, v20
	v_cvt_pk_bf16_f32 v18, v18, s0
	ds_write_b16 v28, v18 offset:4896
	v_or_b32_e32 v18, 3, v26
	v_ashrrev_i32_e32 v19, 31, v18
	v_lshlrev_b64 v[18:19], 9, v[18:19]
	v_lshl_add_u64 v[18:19], v[30:31], 0, v[18:19]
	global_store_dword v[18:19], v21, off sc1
	v_cvt_pk_bf16_f32 v18, v21, s0
	ds_write_b16 v28, v18 offset:816
	v_mul_f32_e32 v18, v21, v21
	v_cvt_pk_bf16_f32 v18, v18, s0
	v_max3_f32 v20, v27, |v20|, |v21|
	ds_write_b16 v28, v18 offset:5168
	v_mov_b32_e32 v18, v107
	v_mov_b32_e32 v19, v107
	v_cmp_eq_u32_e32 vcc, 0, v126
	v_mov_b32_dpp v18, v20 quad_perm:[1,0,3,2] row_mask:0xf bank_mask:0xf
	v_max_f32_e32 v18, v18, v18
	v_max_f32_e32 v18, v20, v18
	s_nop 1
	v_mov_b32_dpp v19, v18 quad_perm:[2,3,0,1] row_mask:0xf bank_mask:0xf
	v_max_f32_e32 v19, v19, v19
	v_max_f32_e32 v18, v18, v19
	v_mov_b32_e32 v19, v107
	s_nop 1
	v_mov_b32_dpp v19, v18 row_half_mirror row_mask:0xf bank_mask:0xf
	v_max_f32_e32 v19, v19, v19
	v_max_f32_e32 v18, v18, v19
	v_mov_b32_e32 v19, v107
	s_nop 1
	v_mov_b32_dpp v19, v18 row_mirror row_mask:0xf bank_mask:0xf
	v_max_f32_e32 v19, v19, v19
	v_max_f32_e32 v18, v18, v19
	s_nop 0
	v_readlane_b32 s8, v18, 0
	v_readlane_b32 s9, v18, 16
	v_readlane_b32 s10, v18, 32
	v_readlane_b32 s11, v18, 48
	v_and_b32_e32 v18, 0x7fffffff, v129
	s_nop 1
	v_add_f32_dpp v18, v18, |v129| quad_perm:[1,0,3,2] row_mask:0xf bank_mask:0xf bound_ctrl:1
	s_nop 1
	v_add_f32_dpp v18, v18, v18 quad_perm:[2,3,0,1] row_mask:0xf bank_mask:0xf bound_ctrl:1
	s_nop 1
	v_add_f32_dpp v18, v18, v18 row_half_mirror row_mask:0xf bank_mask:0xf bound_ctrl:1
	s_nop 1
	v_mov_b32_dpp v107, v18 row_mirror row_mask:0xf bank_mask:0xf
	s_and_saveexec_b64 s[4:5], vcc
	s_cbranch_execz .LBB0_27
	v_mov_b32_e32 v19, 0x1d800
	v_lshl_or_b32 v20, v128, 6, v19
	v_add_f32_e32 v19, v18, v107
	v_max_f32_e64 v18, s11, s11
	v_max_f32_e64 v21, s10, s10
	v_max_f32_e32 v18, v21, v18
	v_mov_b32_e32 v21, s9
	v_max3_f32 v18, s8, v21, v18
	ds_write_b64 v20, v[18:19]
